# v060
# speedup vs baseline: 1.1403x; 1.0005x over previous
.LBB0_4:
	global_load_dwordx4 v[8:11], v[6:7], off
	global_load_dwordx4 v[14:17], v[6:7], off offset:16
	global_load_dwordx4 v[18:21], v[6:7], off offset:32
	global_load_dwordx4 v[22:25], v[6:7], off offset:48
	v_mov_b32_e32 v27, 0xc4b8aa3b
	v_mov_b32_e32 v28, 0xc538aa3b
	v_cmp_eq_u32_e32 vcc, 2, v12
	v_mov_b32_e32 v13, 0
	s_mov_b32 s2, 0xc3e00000
	v_cndmask_b32_e32 v12, v27, v28, vcc
	v_mov_b32_e32 v29, 0x43e00000
	v_lshrrev_b32_e32 v26, 7, v4
	v_mov_b32_e32 v4, 0
	v_mov_b32_e32 v5, 0
	v_mov_b32_e32 v6, 0
	v_mov_b32_e32 v7, 0
	s_load_dwordx2 s[0:1], s[0:1], 0x18
	v_lshlrev_b64 v[2:3], 23, v[2:3]
	v_lshlrev_b32_e32 v26, 11, v26
	s_waitcnt lgkmcnt(0)
	v_lshl_add_u64 v[2:3], s[0:1], 0, v[2:3]
	s_waitcnt vmcnt(3)
	v_pk_mul_f32 v[8:9], v[12:13], v[8:9] op_sel_hi:[0,1]
	s_waitcnt vmcnt(2)
	v_pk_mul_f32 v[16:17], v[12:13], v[16:17] op_sel_hi:[0,1]
	v_pk_mul_f32 v[14:15], v[12:13], v[14:15] op_sel_hi:[0,1]
	s_waitcnt vmcnt(1)
	v_pk_mul_f32 v[20:21], v[12:13], v[20:21] op_sel_hi:[0,1]
	v_pk_mul_f32 v[18:19], v[12:13], v[18:19] op_sel_hi:[0,1]
	s_waitcnt vmcnt(0)
	v_pk_mul_f32 v[22:23], v[12:13], v[22:23] op_sel_hi:[0,1]
	v_pk_mul_f32 v[10:11], v[12:13], v[10:11] op_sel_hi:[0,1]
	v_pk_mul_f32 v[24:25], v[12:13], v[24:25] op_sel_hi:[0,1]
	v_med3_f32 v8, v8, s2, v29
	v_med3_f32 v9, v9, s2, v29
	v_med3_f32 v12, v14, s2, v29
	v_med3_f32 v14, v15, s2, v29
	v_med3_f32 v15, v16, s2, v29
	v_med3_f32 v16, v17, s2, v29
	v_med3_f32 v17, v18, s2, v29
	v_med3_f32 v18, v19, s2, v29
	v_med3_f32 v19, v20, s2, v29
	v_med3_f32 v20, v21, s2, v29
	v_med3_f32 v21, v22, s2, v29
	v_med3_f32 v22, v23, s2, v29
	v_cvt_pk_fp8_f32 v4, v8, v9
	v_cvt_pk_fp8_f32 v5, v12, v14
	v_cvt_pk_fp8_f32 v6, v17, v18
	v_cvt_pk_fp8_f32 v7, v21, v22
	v_med3_f32 v10, v10, s2, v29
	v_med3_f32 v11, v11, s2, v29
	v_med3_f32 v23, v24, s2, v29
	v_med3_f32 v24, v25, s2, v29
	v_cvt_pk_fp8_f32 v4, v10, v11 op_sel:[0,0,1]
	v_cvt_pk_fp8_f32 v5, v15, v16 op_sel:[0,0,1]
	v_cvt_pk_fp8_f32 v6, v19, v20 op_sel:[0,0,1]
	v_cvt_pk_fp8_f32 v7, v23, v24 op_sel:[0,0,1]
	v_and_b32_e32 v12, 0x7ff800, v26
	v_lshl_add_u64 v[2:3], v[2:3], 0, v[12:13]
	v_lshl_add_u64 v[0:1], v[2:3], 0, v[0:1]
	global_store_dwordx4 v[0:1], v[4:7], off sc1

.LBB2_4:
	v_add_u32_e32 v2, s26, v1
	v_add_u32_e32 v29, s24, v1
	v_cmp_gt_u32_e32 vcc, s3, v2
	s_waitcnt vmcnt(2)
	v_bfe_u32 v8, v29, 7, 4
	v_cndmask_b32_e32 v21, v29, v2, vcc
	v_lshrrev_b32_e32 v2, 19, v21
	v_add_u32_e32 v22, s15, v2
	v_lshlrev_b32_e32 v2, 4, v21
	v_and_b32_e32 v20, 0x7f0, v2
	v_bfe_u32 v2, v21, 11, 1
	v_lshrrev_b32_e32 v4, 13, v21
	v_and_or_b32 v28, v4, 2, v2
	v_lshrrev_b32_e32 v2, 9, v21
	v_and_b32_e32 v2, 0x3c0, v2
	v_lshrrev_b32_e32 v4, 8, v21
	v_bfe_u32 v3, v21, 7, 4
	v_lshl_or_b32 v2, v28, 10, v2
	v_and_b32_e32 v4, 48, v4
	v_lshlrev_b32_e32 v18, 2, v20
	v_or3_b32 v6, v2, v4, v3
	v_lshl_add_u64 v[4:5], s[16:17], 0, v[18:19]
	v_lshl_add_u64 v[2:3], s[10:11], 0, v[18:19]
	v_lshl_add_u64 v[4:5], v[4:5], 0, s[20:21]
	v_cmp_gt_u32_e64 s[4:5], s27, v20
	v_ashrrev_i32_e32 v23, 31, v22
	v_lshlrev_b32_e32 v18, 10, v6
	v_cndmask_b32_e64 v3, v5, v3, s[4:5]
	v_cndmask_b32_e64 v2, v4, v2, s[4:5]
	v_lshlrev_b64 v[4:5], 24, v[22:23]
	v_lshl_add_u64 v[2:3], v[2:3], 0, v[4:5]
	v_lshl_add_u64 v[2:3], v[18:19], 2, v[2:3]
	v_and_b32_e32 v18, 0x7f0, v24
	v_lshlrev_b32_e32 v4, 2, v18
	v_mov_b32_e32 v5, v19
	v_lshl_add_u64 v[6:7], s[10:11], 0, v[4:5]
	v_lshl_add_u64 v[4:5], s[16:17], 0, v[4:5]
	v_lshl_add_u64 v[4:5], v[4:5], 0, s[20:21]
	v_cmp_gt_u32_e64 s[4:5], s27, v18
	v_lshl_add_u64 v[46:47], v[2:3], 0, s[22:23]
	s_nop 0
	v_cndmask_b32_e64 v4, v4, v6, s[4:5]
	v_lshrrev_b32_e32 v6, 19, v29
	v_add_u32_e32 v50, s15, v6
	v_ashrrev_i32_e32 v51, 31, v50
	v_cndmask_b32_e64 v5, v5, v7, s[4:5]
	v_lshlrev_b64 v[6:7], 24, v[50:51]
	v_lshl_add_u64 v[4:5], v[4:5], 0, v[6:7]
	v_lshrrev_b32_e32 v6, 13, v29
	v_bfe_u32 v7, v29, 11, 1
	v_and_or_b32 v52, v6, 2, v7
	v_lshrrev_b32_e32 v6, 9, v29
	v_and_b32_e32 v6, 0x3c0, v6
	v_lshrrev_b32_e32 v7, 8, v29
	v_lshl_or_b32 v6, v52, 10, v6
	v_and_b32_e32 v7, 48, v7
	v_or3_b32 v6, v6, v7, v8
	v_lshlrev_b32_e32 v6, 10, v6
	v_mov_b32_e32 v7, v19
	v_lshl_add_u64 v[4:5], v[6:7], 2, v[4:5]
	v_add_co_u32_e64 v6, s[4:5], s28, v4
	v_lshlrev_b32_e32 v29, 4, v29
	s_nop 0
	v_addc_co_u32_e64 v7, s[4:5], -1, v5, s[4:5]
	v_lshl_add_u64 v[4:5], v[4:5], 0, s[22:23]
	global_load_dwordx4 v[30:33], v[6:7], off
	global_load_dwordx4 v[34:37], v[4:5], off offset:16
	global_load_dwordx4 v[38:41], v[4:5], off offset:32
	global_load_dwordx4 v[42:45], v[4:5], off offset:48
	v_add_co_u32_e64 v48, s[4:5], s28, v2
	s_nop 1
	v_addc_co_u32_e64 v49, s[4:5], -1, v3, s[4:5]
	global_load_dwordx4 v[14:17], v[48:49], off
	global_load_dwordx4 v[2:5], v[46:47], off offset:48
	global_load_dwordx4 v[6:9], v[46:47], off offset:32
	global_load_dwordx4 v[10:13], v[46:47], off offset:16
	v_cmp_eq_u32_e64 s[4:5], 2, v52
	v_mov_b32_e32 v48, v19
	v_mov_b32_e32 v46, v19
	v_cndmask_b32_e64 v52, v25, v26, s[4:5]
	v_mov_b32_e32 v47, v19
	v_mov_b32_e32 v49, v19
	s_waitcnt vmcnt(6)
	v_pk_mul_f32 v[34:35], v[34:35], v[52:53] op_sel_hi:[1,0]
	s_waitcnt vmcnt(5)
	v_pk_mul_f32 v[38:39], v[38:39], v[52:53] op_sel_hi:[1,0]
	v_pk_mul_f32 v[30:31], v[30:31], v[52:53] op_sel_hi:[1,0]
	v_med3_f32 v38, v38, s29, v27
	v_med3_f32 v39, v39, s29, v27
	v_cvt_pk_fp8_f32 v48, v38, v39
	v_pk_mul_f32 v[40:41], v[40:41], v[52:53] op_sel_hi:[1,0]
	v_med3_f32 v30, v30, s29, v27
	v_med3_f32 v31, v31, s29, v27
	v_med3_f32 v40, v40, s29, v27
	v_cvt_pk_fp8_f32 v46, v30, v31
	v_med3_f32 v30, v41, s29, v27
	v_cvt_pk_fp8_f32 v48, v40, v30 op_sel:[0,0,1]
	s_waitcnt vmcnt(4)
	v_pk_mul_f32 v[30:31], v[42:43], v[52:53] op_sel_hi:[1,0]
	v_med3_f32 v34, v34, s29, v27
	v_med3_f32 v35, v35, s29, v27
	v_med3_f32 v30, v30, s29, v27
	v_med3_f32 v31, v31, s29, v27
	v_cvt_pk_fp8_f32 v47, v34, v35
	v_cvt_pk_fp8_f32 v49, v30, v31
	v_pk_mul_f32 v[32:33], v[32:33], v[52:53] op_sel_hi:[1,0]
	v_pk_mul_f32 v[36:37], v[36:37], v[52:53] op_sel_hi:[1,0]
	v_pk_mul_f32 v[30:31], v[44:45], v[52:53] op_sel_hi:[1,0]
	v_med3_f32 v32, v32, s29, v27
	v_med3_f32 v33, v33, s29, v27
	v_med3_f32 v36, v36, s29, v27
	v_med3_f32 v37, v37, s29, v27
	v_med3_f32 v30, v30, s29, v27
	v_med3_f32 v31, v31, s29, v27
	v_cvt_pk_fp8_f32 v46, v32, v33 op_sel:[0,0,1]
	v_cvt_pk_fp8_f32 v47, v36, v37 op_sel:[0,0,1]
	v_cvt_pk_fp8_f32 v49, v30, v31 op_sel:[0,0,1]
	v_lshlrev_b64 v[30:31], 23, v[50:51]
	v_and_b32_e32 v32, 0x7ff800, v29
	v_mov_b32_e32 v33, v19
	v_lshl_add_u64 v[30:31], s[8:9], 0, v[30:31]
	v_lshl_add_u64 v[30:31], v[30:31], 0, v[32:33]
	v_lshl_add_u64 v[30:31], v[30:31], 0, v[18:19]
	global_store_dwordx4 v[30:31], v[46:49], off sc1
	s_and_saveexec_b64 s[4:5], vcc
	s_cbranch_execz .LBB2_3
	v_cmp_eq_u32_e32 vcc, 2, v28
	v_lshrrev_b32_e32 v18, 7, v21
	v_lshlrev_b32_e32 v18, 11, v18
	v_cndmask_b32_e32 v28, v25, v26, vcc
	s_waitcnt vmcnt(4)
	v_pk_mul_f32 v[14:15], v[14:15], v[28:29] op_sel_hi:[1,0]
	v_lshlrev_b64 v[22:23], 23, v[22:23]
	v_med3_f32 v29, v14, s29, v27
	v_med3_f32 v15, v15, s29, v27
	v_mov_b32_e32 v14, v19
	v_cvt_pk_fp8_f32 v14, v29, v15
	v_pk_mul_f32 v[16:17], v[16:17], v[28:29] op_sel_hi:[1,0]
	s_waitcnt vmcnt(1)
	v_pk_mul_f32 v[10:11], v[10:11], v[28:29] op_sel_hi:[1,0]
	v_med3_f32 v15, v16, s29, v27
	v_med3_f32 v16, v17, s29, v27
	v_pk_mul_f32 v[6:7], v[6:7], v[28:29] op_sel_hi:[1,0]
	v_pk_mul_f32 v[2:3], v[2:3], v[28:29] op_sel_hi:[1,0]
	v_cvt_pk_fp8_f32 v14, v15, v16 op_sel:[0,0,1]
	v_med3_f32 v10, v10, s29, v27
	v_med3_f32 v11, v11, s29, v27
	v_mov_b32_e32 v15, v19
	v_med3_f32 v6, v6, s29, v27
	v_med3_f32 v7, v7, s29, v27
	v_mov_b32_e32 v16, v19
	v_med3_f32 v2, v2, s29, v27
	v_med3_f32 v3, v3, s29, v27
	v_mov_b32_e32 v17, v19
	v_cvt_pk_fp8_f32 v15, v10, v11
	v_cvt_pk_fp8_f32 v16, v6, v7
	v_cvt_pk_fp8_f32 v17, v2, v3
	v_pk_mul_f32 v[10:11], v[12:13], v[28:29] op_sel_hi:[1,0]
	v_pk_mul_f32 v[6:7], v[8:9], v[28:29] op_sel_hi:[1,0]
	v_pk_mul_f32 v[2:3], v[4:5], v[28:29] op_sel_hi:[1,0]
	v_med3_f32 v10, v10, s29, v27
	v_med3_f32 v11, v11, s29, v27
	v_med3_f32 v6, v6, s29, v27
	v_med3_f32 v7, v7, s29, v27
	v_med3_f32 v2, v2, s29, v27
	v_med3_f32 v3, v3, s29, v27
	v_cvt_pk_fp8_f32 v15, v10, v11 op_sel:[0,0,1]
	v_cvt_pk_fp8_f32 v16, v6, v7 op_sel:[0,0,1]
	v_cvt_pk_fp8_f32 v17, v2, v3 op_sel:[0,0,1]
	v_and_b32_e32 v18, 0x7ff800, v18
	v_lshl_add_u64 v[2:3], s[8:9], 0, v[22:23]
	v_mov_b32_e32 v21, v19
	v_lshl_add_u64 v[2:3], v[2:3], 0, v[18:19]
	v_lshl_add_u64 v[2:3], v[2:3], 0, v[20:21]
	global_store_dwordx4 v[2:3], v[14:17], off sc1
	s_branch .LBB2_3

.LBB3_2:
	global_load_dwordx4 v[8:11], v[6:7], off offset:-2048
	global_load_dwordx4 v[12:15], v[4:5], off offset:-384
	global_load_dwordx4 v[16:19], v[4:5], off offset:-400
	s_addk_i32 s4, 0x80
	s_cmpk_gt_u32 s4, 0x3df
	s_waitcnt vmcnt(1)
	v_cvt_pk_f16_f32 v22, v12, v13
	s_waitcnt vmcnt(0)
	v_cvt_f16_f32_e32 v3, v16
	v_cvt_f16_f32_e32 v21, v17
	v_cvt_pk_f16_f32 v20, v16, v17
	v_cvt_pk_f16_f32 v23, v14, v15
	v_cvt_f32_f16_e32 v3, v3
	v_sub_f32_e32 v3, v16, v3
	v_cvt_f32_f16_e32 v16, v21
	v_cvt_pk_f16_f32 v21, v18, v19
	v_sub_f32_e32 v16, v17, v16
	v_cvt_pk_f16_f32 v24, v3, v16
	v_cvt_f32_f16_e32 v16, v22
	v_cvt_f32_f16_sdwa v17, v22 dst_sel:DWORD dst_unused:UNUSED_PAD src0_sel:WORD_1
	v_mfma_f32_16x16x32_f16 a[0:3], v[8:11], v[20:23], a[0:3]
	v_add_f32_e64 v12, v12, -v16
	v_add_f32_e64 v13, v13, -v17
	v_cvt_pk_f16_f32 v26, v12, v13
	v_cvt_f32_f16_e32 v12, v21
	v_cvt_f32_f16_sdwa v13, v21 dst_sel:DWORD dst_unused:UNUSED_PAD src0_sel:WORD_1
	v_pk_add_f32 v[12:13], v[18:19], v[12:13] neg_lo:[0,1] neg_hi:[0,1]
	s_nop 0
	v_cvt_pk_f16_f32 v25, v12, v13
	v_cvt_f32_f16_e32 v12, v23
	v_cvt_f32_f16_sdwa v13, v23 dst_sel:DWORD dst_unused:UNUSED_PAD src0_sel:WORD_1
	v_pk_add_f32 v[12:13], v[14:15], v[12:13] neg_lo:[0,1] neg_hi:[0,1]
	s_nop 0
	v_cvt_pk_f16_f32 v27, v12, v13
	s_nop 1
	v_mfma_f32_16x16x32_f16 a[0:3], v[8:11], v[24:27], a[0:3]
	global_load_dwordx4 v[8:11], v[6:7], off offset:-1024
	global_load_dwordx4 v[12:15], v[4:5], off offset:-256
	global_load_dwordx4 v[16:19], v[4:5], off offset:-272
	s_waitcnt vmcnt(1)
	v_cvt_pk_f16_f32 v22, v12, v13
	s_waitcnt vmcnt(0)
	v_cvt_f16_f32_e32 v3, v16
	v_cvt_f16_f32_e32 v21, v17
	v_cvt_pk_f16_f32 v20, v16, v17
	v_cvt_pk_f16_f32 v23, v14, v15
	v_cvt_f32_f16_e32 v3, v3
	v_sub_f32_e32 v3, v16, v3
	v_cvt_f32_f16_e32 v16, v21
	v_cvt_pk_f16_f32 v21, v18, v19
	v_sub_f32_e32 v16, v17, v16
	v_cvt_pk_f16_f32 v24, v3, v16
	v_cvt_f32_f16_e32 v16, v22
	v_cvt_f32_f16_sdwa v17, v22 dst_sel:DWORD dst_unused:UNUSED_PAD src0_sel:WORD_1
	v_mfma_f32_16x16x32_f16 a[0:3], v[8:11], v[20:23], a[0:3]
	v_add_f32_e64 v12, v12, -v16
	v_add_f32_e64 v13, v13, -v17
	v_cvt_pk_f16_f32 v26, v12, v13
	v_cvt_f32_f16_e32 v12, v21
	v_cvt_f32_f16_sdwa v13, v21 dst_sel:DWORD dst_unused:UNUSED_PAD src0_sel:WORD_1
	v_pk_add_f32 v[12:13], v[18:19], v[12:13] neg_lo:[0,1] neg_hi:[0,1]
	s_nop 0
	v_cvt_pk_f16_f32 v25, v12, v13
	v_cvt_f32_f16_e32 v12, v23
	v_cvt_f32_f16_sdwa v13, v23 dst_sel:DWORD dst_unused:UNUSED_PAD src0_sel:WORD_1
	v_pk_add_f32 v[12:13], v[14:15], v[12:13] neg_lo:[0,1] neg_hi:[0,1]
	s_nop 0
	v_cvt_pk_f16_f32 v27, v12, v13
	s_nop 1
	v_mfma_f32_16x16x32_f16 a[0:3], v[8:11], v[24:27], a[0:3]
	global_load_dwordx4 v[8:11], v[6:7], off
	global_load_dwordx4 v[12:15], v[4:5], off offset:-128
	global_load_dwordx4 v[16:19], v[4:5], off offset:-144
	s_waitcnt vmcnt(1)
	v_cvt_pk_f16_f32 v22, v12, v13
	s_waitcnt vmcnt(0)
	v_cvt_f16_f32_e32 v3, v16
	v_cvt_f16_f32_e32 v21, v17
	v_cvt_pk_f16_f32 v20, v16, v17
	v_cvt_pk_f16_f32 v23, v14, v15
	v_cvt_f32_f16_e32 v3, v3
	v_sub_f32_e32 v3, v16, v3
	v_cvt_f32_f16_e32 v16, v21
	v_cvt_pk_f16_f32 v21, v18, v19
	v_sub_f32_e32 v16, v17, v16
	v_cvt_pk_f16_f32 v24, v3, v16
	v_cvt_f32_f16_e32 v16, v22
	v_cvt_f32_f16_sdwa v17, v22 dst_sel:DWORD dst_unused:UNUSED_PAD src0_sel:WORD_1
	v_mfma_f32_16x16x32_f16 a[0:3], v[8:11], v[20:23], a[0:3]
	v_add_f32_e64 v12, v12, -v16
	v_add_f32_e64 v13, v13, -v17
	v_cvt_pk_f16_f32 v26, v12, v13
	v_cvt_f32_f16_e32 v12, v21
	v_cvt_f32_f16_sdwa v13, v21 dst_sel:DWORD dst_unused:UNUSED_PAD src0_sel:WORD_1
	v_pk_add_f32 v[12:13], v[18:19], v[12:13] neg_lo:[0,1] neg_hi:[0,1]
	s_nop 0
	v_cvt_pk_f16_f32 v25, v12, v13
	v_cvt_f32_f16_e32 v12, v23
	v_cvt_f32_f16_sdwa v13, v23 dst_sel:DWORD dst_unused:UNUSED_PAD src0_sel:WORD_1
	v_pk_add_f32 v[12:13], v[14:15], v[12:13] neg_lo:[0,1] neg_hi:[0,1]
	s_nop 0
	v_cvt_pk_f16_f32 v27, v12, v13
	s_nop 1
	v_mfma_f32_16x16x32_f16 a[0:3], v[8:11], v[24:27], a[0:3]
	global_load_dwordx4 v[8:11], v[6:7], off offset:1024
	global_load_dwordx4 v[12:15], v[4:5], off
	global_load_dwordx4 v[16:19], v[4:5], off offset:-16
	v_lshl_add_u64 v[4:5], v[4:5], 0, s[0:1]
	v_lshl_add_u64 v[6:7], v[6:7], 0, s[2:3]
	s_waitcnt vmcnt(1)
	v_cvt_pk_f16_f32 v22, v12, v13
	s_waitcnt vmcnt(0)
	v_cvt_f16_f32_e32 v3, v16
	v_cvt_f16_f32_e32 v21, v17
	v_cvt_pk_f16_f32 v20, v16, v17
	v_cvt_pk_f16_f32 v23, v14, v15
	v_cvt_f32_f16_e32 v3, v3
	v_sub_f32_e32 v3, v16, v3
	v_cvt_f32_f16_e32 v16, v21
	v_cvt_pk_f16_f32 v21, v18, v19
	v_sub_f32_e32 v16, v17, v16
	v_cvt_pk_f16_f32 v24, v3, v16
	v_cvt_f32_f16_e32 v16, v22
	v_cvt_f32_f16_sdwa v17, v22 dst_sel:DWORD dst_unused:UNUSED_PAD src0_sel:WORD_1
	v_mfma_f32_16x16x32_f16 a[0:3], v[8:11], v[20:23], a[0:3]
	v_add_f32_e64 v12, v12, -v16
	v_add_f32_e64 v13, v13, -v17
	v_cvt_pk_f16_f32 v26, v12, v13
	v_cvt_f32_f16_e32 v12, v21
	v_cvt_f32_f16_sdwa v13, v21 dst_sel:DWORD dst_unused:UNUSED_PAD src0_sel:WORD_1
	v_pk_add_f32 v[12:13], v[18:19], v[12:13] neg_lo:[0,1] neg_hi:[0,1]
	s_nop 0
	v_cvt_pk_f16_f32 v25, v12, v13
	v_cvt_f32_f16_e32 v12, v23
	v_cvt_f32_f16_sdwa v13, v23 dst_sel:DWORD dst_unused:UNUSED_PAD src0_sel:WORD_1
	v_pk_add_f32 v[12:13], v[14:15], v[12:13] neg_lo:[0,1] neg_hi:[0,1]
	s_nop 0
	v_cvt_pk_f16_f32 v27, v12, v13
	s_nop 1
	v_mfma_f32_16x16x32_f16 a[0:3], v[8:11], v[24:27], a[0:3]
	s_cbranch_scc0 .LBB3_2
	v_lshlrev_b32_e32 v4, 2, v2
	global_load_dword v4, v4, s[8:9]
	v_lshlrev_b32_e32 v0, 2, v0
	v_lshlrev_b32_e32 v5, 4, v1
	v_and_b32_e32 v0, 0xc0, v0
	s_nop 1
	v_accvgpr_read_b32 v10, a0
	v_mov_b32_e32 v1, 0
	v_or3_b32 v0, v0, v5, v2
	v_accvgpr_read_b32 v9, a1
	v_accvgpr_read_b32 v8, a2
	v_accvgpr_read_b32 v3, a3
	v_lshl_add_u64 v[0:1], v[0:1], 2, s[10:11]
	s_waitcnt vmcnt(0)
	v_add_f32_e32 v2, v4, v10
	v_add_f32_e32 v5, v4, v9
	v_add_f32_e32 v6, v4, v8
	v_add_f32_e32 v3, v4, v3
	global_store_dword v[0:1], v2, off sc1
	global_store_dword v[0:1], v5, off offset:64 sc1
	global_store_dword v[0:1], v6, off offset:128 sc1
	global_store_dword v[0:1], v3, off offset:192 sc1
